# dsa_build_q: the 8 indexer-query row loads issued together once (were 4 dependent round trips plus a reload)
# speedup vs baseline: 1.0098x; 1.0098x over previous
.LBB0_497:
	s_or_b64 exec, exec, s[0:1]
	s_mul_i32 s0, s44, 0x1200000
	s_mul_hi_i32 s1, s44, 0x1200000
	s_add_u32 s0, s74, s0
	s_addc_u32 s1, s75, s1
	s_add_i32 s12, 0, 0x23400
	v_ashrrev_i32_e32 v54, 4, v42
	v_mov_b32_e32 v0, s12
	s_lshl_b32 s49, s30, 6
	v_readlane_b32 s13, v252, 19
	v_and_b32_e32 v232, 15, v42
	s_waitcnt lgkmcnt(0)
	s_barrier
	ds_read_b128 v[6:9], v0
	ds_read_b128 v[2:5], v0 offset:16
	s_or_b32 s12, s49, s13
	v_mov_b32_e32 v0, v54
	v_or_b32_e32 v44, s12, v232
	v_mov_b64_e32 v[10:11], s[0:1]
	v_lshlrev_b32_e32 v12, 3, v0
	v_mad_i64_i32 v[10:11], s[0:1], v44, s2, v[10:11]
	v_ashrrev_i32_e32 v13, 31, v12
	v_lshl_add_u64 v[38:39], v[12:13], 1, v[10:11]
	global_load_dwordx4 v[10:13], v[38:39], off offset:2048
	global_load_dwordx4 v[14:17], v[38:39], off offset:2112
	v_ashrrev_i32_e32 v45, 31, v44
	v_lshlrev_b64 v[18:19], 9, v[44:45]
	v_lshl_add_u64 v[18:19], s[42:43], 0, v[18:19]
	global_load_dwordx2 v[50:51], v[18:19], off offset:384
	global_load_dwordx4 v[72:75], v[38:39], off offset:2048
	global_load_dwordx4 v[76:79], v[38:39], off offset:2112
	global_load_dwordx4 v[80:83], v[38:39], off offset:2176
	global_load_dwordx4 v[84:87], v[38:39], off offset:2240
	global_load_dwordx4 v[88:91], v[38:39], off offset:2304
	global_load_dwordx4 v[92:95], v[38:39], off offset:2368
	global_load_dwordx4 v[96:99], v[38:39], off offset:2432
	global_load_dwordx4 v[100:103], v[38:39], off offset:2496
	v_ashrrev_i32_e32 v233, 3, v42
	v_readlane_b32 s12, v251, 50
	s_add_u32 s0, s42, 0x100
	s_addc_u32 s1, s43, 0
	v_add_u32_e32 v46, s12, v233
	v_ashrrev_i32_e32 v47, 31, v46
	v_lshlrev_b64 v[46:47], 9, v[46:47]
	s_movk_i32 s12, 0x70
	s_mov_b64 s[16:17], 0x8000
	s_add_i32 s30, s30, 2
	s_ashr_i32 s50, s30, 1
	v_ashrrev_i32_e32 v43, 31, v42
	s_waitcnt vmcnt(2)
	v_lshlrev_b32_e32 v0, 16, v10
	v_and_b32_e32 v10, 0xffff0000, v10
	v_lshlrev_b32_e32 v18, 16, v11
	v_and_b32_e32 v11, 0xffff0000, v11
	v_lshlrev_b32_e32 v19, 16, v12
	v_and_b32_e32 v12, 0xffff0000, v12
	v_mul_f32_e32 v10, v10, v10
	v_mul_f32_e32 v11, v11, v11
	v_lshlrev_b32_e32 v20, 16, v13
	v_and_b32_e32 v13, 0xffff0000, v13
	v_mul_f32_e32 v12, v12, v12
	v_fmac_f32_e32 v10, v0, v0
	v_fmac_f32_e32 v11, v18, v18
	s_waitcnt vmcnt(1)
	v_lshlrev_b32_e32 v21, 16, v14
	v_and_b32_e32 v14, 0xffff0000, v14
	v_mul_f32_e32 v13, v13, v13
	v_fmac_f32_e32 v12, v19, v19
	v_add_f32_e32 v0, v10, v11
	v_lshlrev_b32_e32 v22, 16, v15
	v_and_b32_e32 v15, 0xffff0000, v15
	v_mul_f32_e32 v14, v14, v14
	v_fmac_f32_e32 v13, v20, v20
	v_add_f32_e32 v0, v12, v0
	v_lshlrev_b32_e32 v23, 16, v16
	v_and_b32_e32 v16, 0xffff0000, v16
	v_mul_f32_e32 v15, v15, v15
	v_fmac_f32_e32 v14, v21, v21
	v_add_f32_e32 v0, v13, v0
	v_lshlrev_b32_e32 v24, 16, v17
	v_and_b32_e32 v17, 0xffff0000, v17
	v_mul_f32_e32 v16, v16, v16
	v_fmac_f32_e32 v15, v22, v22
	v_add_f32_e32 v0, v14, v0
	v_mul_f32_e32 v17, v17, v17
	v_fmac_f32_e32 v16, v23, v23
	v_add_f32_e32 v0, v15, v0
	v_fmac_f32_e32 v17, v24, v24
	v_add_f32_e32 v0, v16, v0
	v_add_f32_e32 v0, v17, v0
	v_mov_b32_e32 v10, v0
	s_nop 1
	v_permlane16_swap_b32_e32 v0, v10
	v_add_f32_e32 v56, v0, v10
	v_mov_b32_e32 v57, v56
	v_mov_b64_e32 v[10:11], v[80:81]
	v_mov_b64_e32 v[12:13], v[82:83]
	v_mov_b64_e32 v[14:15], v[84:85]
	v_mov_b64_e32 v[16:17], v[86:87]
	v_permlane32_swap_b32_e32 v56, v57
	s_waitcnt vmcnt(1)
	v_lshlrev_b32_e32 v0, 16, v10
	v_and_b32_e32 v10, 0xffff0000, v10
	v_lshlrev_b32_e32 v18, 16, v11
	v_and_b32_e32 v11, 0xffff0000, v11
	v_lshlrev_b32_e32 v19, 16, v12
	v_and_b32_e32 v12, 0xffff0000, v12
	v_mul_f32_e32 v10, v10, v10
	v_mul_f32_e32 v11, v11, v11
	v_lshlrev_b32_e32 v20, 16, v13
	v_and_b32_e32 v13, 0xffff0000, v13
	v_mul_f32_e32 v12, v12, v12
	v_fmac_f32_e32 v10, v0, v0
	v_fmac_f32_e32 v11, v18, v18
	s_waitcnt vmcnt(0)
	v_lshlrev_b32_e32 v21, 16, v14
	v_and_b32_e32 v14, 0xffff0000, v14
	v_mul_f32_e32 v13, v13, v13
	v_fmac_f32_e32 v12, v19, v19
	v_add_f32_e32 v0, v10, v11
	v_lshlrev_b32_e32 v22, 16, v15
	v_and_b32_e32 v15, 0xffff0000, v15
	v_mul_f32_e32 v14, v14, v14
	v_fmac_f32_e32 v13, v20, v20
	v_add_f32_e32 v0, v12, v0
	v_lshlrev_b32_e32 v23, 16, v16
	v_and_b32_e32 v16, 0xffff0000, v16
	v_mul_f32_e32 v15, v15, v15
	v_fmac_f32_e32 v14, v21, v21
	v_add_f32_e32 v0, v13, v0
	v_lshlrev_b32_e32 v24, 16, v17
	v_and_b32_e32 v17, 0xffff0000, v17
	v_mul_f32_e32 v16, v16, v16
	v_fmac_f32_e32 v15, v22, v22
	v_add_f32_e32 v0, v14, v0
	v_mul_f32_e32 v17, v17, v17
	v_fmac_f32_e32 v16, v23, v23
	v_add_f32_e32 v0, v15, v0
	v_fmac_f32_e32 v17, v24, v24
	v_add_f32_e32 v0, v16, v0
	v_add_f32_e32 v0, v17, v0
	v_mov_b32_e32 v10, v0
	s_nop 1
	v_permlane16_swap_b32_e32 v0, v10
	v_add_f32_e32 v58, v0, v10
	v_mov_b32_e32 v59, v58
	v_mov_b64_e32 v[10:11], v[88:89]
	v_mov_b64_e32 v[12:13], v[90:91]
	v_mov_b64_e32 v[14:15], v[92:93]
	v_mov_b64_e32 v[16:17], v[94:95]
	v_permlane32_swap_b32_e32 v58, v59
	s_waitcnt vmcnt(1)
	v_lshlrev_b32_e32 v0, 16, v10
	v_and_b32_e32 v10, 0xffff0000, v10
	v_lshlrev_b32_e32 v18, 16, v11
	v_and_b32_e32 v11, 0xffff0000, v11
	v_lshlrev_b32_e32 v19, 16, v12
	v_and_b32_e32 v12, 0xffff0000, v12
	v_mul_f32_e32 v10, v10, v10
	v_mul_f32_e32 v11, v11, v11
	v_lshlrev_b32_e32 v20, 16, v13
	v_and_b32_e32 v13, 0xffff0000, v13
	v_mul_f32_e32 v12, v12, v12
	v_fmac_f32_e32 v10, v0, v0
	v_fmac_f32_e32 v11, v18, v18
	s_waitcnt vmcnt(0)
	v_lshlrev_b32_e32 v21, 16, v14
	v_and_b32_e32 v14, 0xffff0000, v14
	v_mul_f32_e32 v13, v13, v13
	v_fmac_f32_e32 v12, v19, v19
	v_add_f32_e32 v0, v10, v11
	v_lshlrev_b32_e32 v22, 16, v15
	v_and_b32_e32 v15, 0xffff0000, v15
	v_mul_f32_e32 v14, v14, v14
	v_fmac_f32_e32 v13, v20, v20
	v_add_f32_e32 v0, v12, v0
	v_lshlrev_b32_e32 v23, 16, v16
	v_and_b32_e32 v16, 0xffff0000, v16
	v_mul_f32_e32 v15, v15, v15
	v_fmac_f32_e32 v14, v21, v21
	v_add_f32_e32 v0, v13, v0
	v_lshlrev_b32_e32 v24, 16, v17
	v_and_b32_e32 v17, 0xffff0000, v17
	v_mul_f32_e32 v16, v16, v16
	v_fmac_f32_e32 v15, v22, v22
	v_add_f32_e32 v0, v14, v0
	v_mul_f32_e32 v17, v17, v17
	v_fmac_f32_e32 v16, v23, v23
	v_add_f32_e32 v0, v15, v0
	v_fmac_f32_e32 v17, v24, v24
	v_add_f32_e32 v0, v16, v0
	v_add_f32_e32 v0, v17, v0
	v_mov_b32_e32 v10, v0
	s_nop 1
	v_permlane16_swap_b32_e32 v0, v10
	v_add_f32_e32 v60, v0, v10
	v_mov_b32_e32 v61, v60
	v_mov_b64_e32 v[10:11], v[96:97]
	v_mov_b64_e32 v[12:13], v[98:99]
	v_mov_b64_e32 v[14:15], v[100:101]
	v_mov_b64_e32 v[16:17], v[102:103]
	v_permlane32_swap_b32_e32 v60, v61
	s_waitcnt vmcnt(1)
	v_lshlrev_b32_e32 v0, 16, v10
	v_and_b32_e32 v10, 0xffff0000, v10
	v_lshlrev_b32_e32 v18, 16, v11
	v_and_b32_e32 v11, 0xffff0000, v11
	v_lshlrev_b32_e32 v19, 16, v12
	v_and_b32_e32 v12, 0xffff0000, v12
	v_mul_f32_e32 v10, v10, v10
	v_mul_f32_e32 v11, v11, v11
	v_lshlrev_b32_e32 v20, 16, v13
	v_and_b32_e32 v13, 0xffff0000, v13
	v_mul_f32_e32 v12, v12, v12
	v_fmac_f32_e32 v10, v0, v0
	v_fmac_f32_e32 v11, v18, v18
	s_waitcnt vmcnt(0)
	v_lshlrev_b32_e32 v21, 16, v14
	v_and_b32_e32 v14, 0xffff0000, v14
	v_mul_f32_e32 v13, v13, v13
	v_fmac_f32_e32 v12, v19, v19
	v_add_f32_e32 v0, v10, v11
	v_lshlrev_b32_e32 v22, 16, v15
	v_and_b32_e32 v15, 0xffff0000, v15
	v_mul_f32_e32 v14, v14, v14
	v_fmac_f32_e32 v13, v20, v20
	v_add_f32_e32 v0, v12, v0
	v_lshlrev_b32_e32 v23, 16, v16
	v_and_b32_e32 v16, 0xffff0000, v16
	v_mul_f32_e32 v15, v15, v15
	v_fmac_f32_e32 v14, v21, v21
	v_add_f32_e32 v0, v13, v0
	v_lshlrev_b32_e32 v24, 16, v17
	v_and_b32_e32 v17, 0xffff0000, v17
	v_mul_f32_e32 v16, v16, v16
	v_fmac_f32_e32 v15, v22, v22
	v_add_f32_e32 v0, v14, v0
	v_mul_f32_e32 v17, v17, v17
	v_fmac_f32_e32 v16, v23, v23
	v_add_f32_e32 v0, v15, v0
	v_fmac_f32_e32 v17, v24, v24
	v_add_f32_e32 v0, v16, v0
	v_add_f32_e32 v0, v17, v0
	v_mov_b32_e32 v10, v0
	s_nop 1
	v_permlane16_swap_b32_e32 v0, v10
	v_add_f32_e32 v62, v0, v10
	v_mov_b32_e32 v63, v62
	v_mov_b64_e32 v[30:31], v[72:73]
	v_mov_b64_e32 v[32:33], v[74:75]
	v_mov_b64_e32 v[26:27], v[76:77]
	v_mov_b64_e32 v[28:29], v[78:79]
	v_mov_b64_e32 v[22:23], v[80:81]
	v_mov_b64_e32 v[24:25], v[82:83]
	v_mov_b64_e32 v[18:19], v[84:85]
	v_mov_b64_e32 v[20:21], v[86:87]
	v_mov_b64_e32 v[14:15], v[88:89]
	v_mov_b64_e32 v[16:17], v[90:91]
	v_mov_b64_e32 v[10:11], v[92:93]
	v_mov_b64_e32 v[12:13], v[94:95]
	v_mov_b64_e32 v[34:35], v[96:97]
	v_mov_b64_e32 v[36:37], v[98:99]
	s_nop 0
	v_mov_b64_e32 v[38:39], v[100:101]
	v_mov_b64_e32 v[40:41], v[102:103]
	v_xor_b32_e32 v0, v233, v42
	v_lshlrev_b32_e32 v0, 4, v0
	v_and_or_b32 v46, v0, s12, v46
	v_lshl_add_u64 v[48:49], v[46:47], 0, s[16:17]
	v_lshl_add_u64 v[64:65], s[0:1], 0, v[46:47]
	s_mov_b32 s12, m0
	s_mov_b32 m0, s93
	s_nop 0
	global_load_lds_dwordx4 v[64:65], off
	s_mov_b32 m0, s12
	v_lshl_add_u64 v[64:65], s[0:1], 0, v[48:49]
	s_add_i32 s0, s93, 0x2000
	s_mov_b32 s1, m0
	s_mov_b32 m0, s0
	s_nop 0
	global_load_lds_dwordx4 v[64:65], off
	s_mov_b32 m0, s1
	s_cmp_gt_i32 s50, 0
	v_permlane32_swap_b32_e32 v62, v63
	s_cselect_b64 s[46:47], -1, 0
	s_cmp_lt_i32 s50, 1
	v_or_b32_e32 v0, s13, v232
	s_cbranch_scc1 .LBB0_510
	s_waitcnt lgkmcnt(1)
	v_mov_b32_e32 v64, v6
	s_waitcnt lgkmcnt(0)
	v_mov_b32_e32 v65, v2
	v_mov_b32_e32 v2, v7
	v_mov_b32_e32 v6, v8
	v_mov_b32_e32 v7, v4
	v_mov_b32_e32 v4, v9
	v_pk_add_f32 v[2:3], v[64:65], v[2:3]
	v_pk_add_f32 v[4:5], v[6:7], v[4:5]
	v_lshlrev_b32_e32 v45, 16, v50
	v_pk_add_f32 v[2:3], v[2:3], v[4:5]
	v_mul_f32_e32 v66, 0x3d800000, v45
	v_add_f32_e32 v2, v2, v3
	v_mul_f32_e32 v2, 0x39000000, v2
	v_mul_f32_e32 v3, 0x4f800000, v2
	v_cmp_gt_f32_e64 s[0:1], s78, v2
	v_and_b32_e32 v45, 0xffff0000, v50
	v_mul_f32_e32 v67, 0x3d800000, v45
	v_cndmask_b32_e64 v2, v2, v3, s[0:1]
	v_sqrt_f32_e32 v3, v2
	s_mov_b32 s12, 0x40400000
	v_cmp_lt_f32_e64 s[30:31], 0, v66
	v_cmp_lt_f32_e32 vcc, 0, v67
	v_add_u32_e32 v4, -1, v3
	v_fma_f32 v5, -v4, v3, v2
	v_cmp_ge_f32_e64 s[40:41], 0, v5
	v_add_u32_e32 v5, 1, v3
	v_lshlrev_b32_e32 v45, 16, v51
	v_cndmask_b32_e64 v4, v3, v4, s[40:41]
	v_fma_f32 v3, -v5, v3, v2
	v_cmp_lt_f32_e64 s[40:41], 0, v3
	v_mul_f32_e32 v68, 0x3d800000, v45
	v_cmp_lt_f32_e64 s[34:35], 0, v68
	v_cndmask_b32_e64 v3, v4, v5, s[40:41]
	v_add_f32_e32 v5, v56, v57
	v_mul_f32_e32 v6, 0x4f800000, v5
	v_cmp_gt_f32_e64 s[40:41], s78, v5
	v_mul_f32_e32 v4, 0x37800000, v3
	v_cndmask_b32_e64 v3, v3, v4, s[0:1]
	v_cndmask_b32_e64 v5, v5, v6, s[40:41]
	v_sqrt_f32_e32 v6, v5
	v_cmp_class_f32_e64 s[0:1], v2, v231
	v_and_b32_e32 v45, 0xffff0000, v51
	v_mul_f32_e32 v69, 0x3d800000, v45
	v_cndmask_b32_e64 v2, v3, v2, s[0:1]
	v_add_u32_e32 v3, -1, v6
	v_fma_f32 v4, -v3, v6, v5
	v_cmp_ge_f32_e64 s[0:1], 0, v4
	v_add_u32_e32 v4, 1, v6
	v_cmp_lt_f32_e64 s[36:37], 0, v69
	v_cndmask_b32_e64 v3, v6, v3, s[0:1]
	v_fma_f32 v6, -v4, v6, v5
	v_cmp_lt_f32_e64 s[0:1], 0, v6
	v_mov_b32_e32 v55, 0xff800000
	v_mov_b32_e32 v70, 0x7f800000
	v_cndmask_b32_e64 v3, v3, v4, s[0:1]
	v_mul_f32_e32 v4, 0x37800000, v3
	v_cndmask_b32_e64 v3, v3, v4, s[40:41]
	v_cmp_class_f32_e64 s[0:1], v5, v231
	v_add_f32_e32 v4, v58, v59
	v_cndmask_b32_e64 v51, v55, 0, vcc
	v_cndmask_b32_e64 v3, v3, v5, s[0:1]
	v_mul_f32_e32 v5, 0x4f800000, v4
	v_cmp_gt_f32_e64 s[0:1], s78, v4
	v_mul_f32_e64 v3, |v66|, v3
	v_mul_f32_e32 v3, v2, v3
	v_cndmask_b32_e64 v4, v4, v5, s[0:1]
	v_sqrt_f32_e32 v5, v4
	v_fma_f32 v3, v3, s12, 0
	v_cndmask_b32_e64 v6, 0, v3, s[30:31]
	v_cndmask_b32_e64 v3, v3, 0, s[30:31]
	v_add_u32_e32 v7, -1, v5
	v_fma_f32 v8, -v7, v5, v4
	v_cmp_ge_f32_e64 s[40:41], 0, v8
	v_add_u32_e32 v8, 1, v5
	s_mov_b32 s12, 0x467c0400
	v_cndmask_b32_e64 v7, v5, v7, s[40:41]
	v_fma_f32 v5, -v8, v5, v4
	v_cmp_lt_f32_e64 s[40:41], 0, v5
	v_cndmask_b32_e64 v45, v55, 0, s[30:31]
	v_cndmask_b32_e64 v50, 0, v70, s[30:31]
	v_cndmask_b32_e64 v5, v7, v8, s[40:41]
	v_mul_f32_e32 v7, 0x37800000, v5
	v_cndmask_b32_e64 v5, v5, v7, s[0:1]
	v_cmp_class_f32_e64 s[0:1], v4, v231
	v_readlane_b32 s30, v251, 39
	v_cndmask_b32_e64 v53, v55, 0, s[34:35]
	v_cndmask_b32_e64 v4, v5, v4, s[0:1]
	v_add_f32_e32 v5, v60, v61
	v_mul_f32_e32 v7, 0x4f800000, v5
	v_cmp_gt_f32_e64 s[0:1], s78, v5
	v_mul_f32_e64 v4, |v67|, v4
	v_mul_f32_e32 v4, v2, v4
	v_cndmask_b32_e64 v5, v5, v7, s[0:1]
	v_sqrt_f32_e32 v7, v5
	v_fmamk_f32 v8, v4, 0x40400000, v6
	v_cndmask_b32_e32 v6, v6, v8, vcc
	v_fmamk_f32 v4, v4, 0x40400000, v3
	v_add_u32_e32 v8, -1, v7
	v_fma_f32 v9, -v8, v7, v5
	v_cmp_ge_f32_e64 s[40:41], 0, v9
	v_add_u32_e32 v9, 1, v7
	v_cndmask_b32_e32 v3, v4, v3, vcc
	v_cndmask_b32_e64 v8, v7, v8, s[40:41]
	v_fma_f32 v7, -v9, v7, v5
	v_cmp_lt_f32_e64 s[40:41], 0, v7
	v_cndmask_b32_e64 v55, v55, 0, s[36:37]
	v_cndmask_b32_e64 v57, 0, v70, s[34:35]
	v_cndmask_b32_e64 v7, v8, v9, s[40:41]
	v_mul_f32_e32 v8, 0x37800000, v7
	v_cndmask_b32_e64 v7, v7, v8, s[0:1]
	v_cmp_class_f32_e64 s[0:1], v5, v231
	v_cndmask_b32_e64 v58, 0, v70, s[36:37]
	s_mov_b32 s13, 0
	v_cndmask_b32_e64 v5, v7, v5, s[0:1]
	v_add_f32_e32 v7, v62, v63
	v_mul_f32_e32 v8, 0x4f800000, v7
	v_cmp_gt_f32_e64 s[0:1], s78, v7
	v_mul_f32_e64 v5, |v68|, v5
	v_mul_f32_e32 v5, v2, v5
	v_cndmask_b32_e64 v7, v7, v8, s[0:1]
	v_sqrt_f32_e32 v8, v7
	v_fmamk_f32 v9, v5, 0x40400000, v6
	v_cndmask_b32_e64 v6, v6, v9, s[34:35]
	v_fmamk_f32 v4, v5, 0x40400000, v3
	v_add_u32_e32 v9, -1, v8
	v_fma_f32 v56, -v9, v8, v7
	v_cmp_ge_f32_e64 s[40:41], 0, v56
	v_add_u32_e32 v56, 1, v8
	v_cndmask_b32_e64 v3, v4, v3, s[34:35]
	v_cndmask_b32_e64 v9, v8, v9, s[40:41]
	v_fma_f32 v8, -v56, v8, v7
	v_cmp_lt_f32_e64 s[40:41], 0, v8
	s_nop 1
	v_cndmask_b32_e64 v8, v9, v56, s[40:41]
	v_mul_f32_e32 v9, 0x37800000, v8
	v_cndmask_b32_e64 v8, v8, v9, s[0:1]
	v_cmp_class_f32_e64 s[0:1], v7, v231
	v_cndmask_b32_e32 v56, 0, v70, vcc
	s_waitcnt vmcnt(0)
	v_and_b32_e32 v9, 0xffff0000, v41
	v_cndmask_b32_e64 v7, v8, v7, s[0:1]
	v_mul_f32_e64 v7, |v69|, v7
	v_mul_f32_e32 v2, v2, v7
	v_fmamk_f32 v7, v2, 0x40400000, v6
	v_fmamk_f32 v2, v2, 0x40400000, v3
	v_cndmask_b32_e64 v6, v6, v7, s[36:37]
	v_cndmask_b32_e64 v2, v2, v3, s[36:37]
	v_max_f32_e32 v2, v6, v2
	v_div_scale_f32 v3, s[0:1], v2, v2, s12
	v_rcp_f32_e32 v4, v3
	v_and_b32_e32 v8, 0xffff0000, v40
	s_movk_i32 s0, 0x70
	v_readlane_b32 s1, v253, 42
	v_fma_f32 v5, -v3, v4, 1.0
	v_fmac_f32_e32 v4, v5, v4
	v_div_scale_f32 v5, vcc, s12, v2, s12
	v_mul_f32_e32 v6, v5, v4
	v_fma_f32 v7, -v3, v6, v5
	v_fmac_f32_e32 v6, v7, v4
	v_fma_f32 v3, -v3, v6, v5
	v_div_fmas_f32 v3, v3, v4, v6
	v_div_fixup_f32 v3, v3, v2, s12
	v_cmp_lt_f32_e32 vcc, 0, v2
	v_and_b32_e32 v2, 0xffff0000, v38
	v_lshlrev_b32_e32 v5, 16, v39
	v_cndmask_b32_e32 v59, 0, v3, vcc
	v_mul_f32_e32 v6, v69, v59
	v_and_b32_e32 v3, 0xffff0000, v39
	v_pk_mul_f32 v[2:3], v[6:7], v[2:3] op_sel_hi:[0,1]
	v_lshlrev_b32_e32 v4, 16, v38
	v_pk_mul_f32 v[8:9], v[6:7], v[8:9] op_sel_hi:[0,1]
	v_lshlrev_b32_e32 v39, 16, v41
	v_lshlrev_b32_e32 v38, 16, v40
	v_pk_mul_f32 v[4:5], v[6:7], v[4:5] op_sel_hi:[0,1]
	v_pk_mul_f32 v[38:39], v[6:7], v[38:39] op_sel_hi:[0,1]
	v_bfe_u32 v7, v9, 16, 1
	v_bfe_u32 v41, v3, 16, 1
	v_bfe_u32 v40, v8, 16, 1
	v_bfe_u32 v60, v2, 16, 1
	v_add3_u32 v3, v3, v41, s39
	v_add3_u32 v7, v9, v7, s39
	v_bfe_u32 v9, v4, 16, 1
	v_bfe_u32 v41, v38, 16, 1
	v_add3_u32 v2, v2, v60, s39
	v_add3_u32 v8, v8, v40, s39
	v_bfe_u32 v40, v5, 16, 1
	v_bfe_u32 v60, v39, 16, 1
	v_add3_u32 v38, v38, v41, s39
	v_add3_u32 v4, v4, v9, s39
	v_add3_u32 v39, v39, v60, s39
	v_add3_u32 v5, v5, v40, s39
	v_lshrrev_b32_e32 v9, 16, v4
	v_lshrrev_b32_e32 v4, 16, v38
	v_lshrrev_b32_e32 v40, 16, v5
	v_lshrrev_b32_e32 v5, 16, v39
	v_and_or_b32 v4, v8, s38, v4
	v_and_or_b32 v2, v2, s38, v9
	v_and_b32_e32 v9, 0xffff0000, v35
	v_and_b32_e32 v8, 0xffff0000, v34
	v_and_b32_e32 v39, 0xffff0000, v37
	v_and_b32_e32 v38, 0xffff0000, v36
	v_pk_mul_f32 v[8:9], v[6:7], v[8:9] op_sel_hi:[0,1]
	v_lshlrev_b32_e32 v35, 16, v35
	v_lshlrev_b32_e32 v34, 16, v34
	v_pk_mul_f32 v[38:39], v[6:7], v[38:39] op_sel_hi:[0,1]
	v_lshlrev_b32_e32 v37, 16, v37
	v_lshlrev_b32_e32 v36, 16, v36
	v_and_or_b32 v5, v7, s38, v5
	v_and_or_b32 v3, v3, s38, v40
	v_pk_mul_f32 v[34:35], v[6:7], v[34:35] op_sel_hi:[0,1]
	v_pk_mul_f32 v[6:7], v[6:7], v[36:37] op_sel_hi:[0,1]
	v_bfe_u32 v36, v39, 16, 1
	v_bfe_u32 v37, v38, 16, 1
	v_bfe_u32 v40, v9, 16, 1
	v_bfe_u32 v41, v8, 16, 1
	v_add3_u32 v41, v8, v41, s39
	v_add3_u32 v40, v9, v40, s39
	v_add3_u32 v8, v38, v37, s39
	v_add3_u32 v9, v39, v36, s39
	v_bfe_u32 v36, v34, 16, 1
	v_bfe_u32 v38, v6, 16, 1
	v_bfe_u32 v37, v35, 16, 1
	v_add3_u32 v6, v6, v38, s39
	v_add3_u32 v34, v34, v36, s39
	v_bfe_u32 v39, v7, 16, 1
	v_add3_u32 v35, v35, v37, s39
	v_lshrrev_b32_e32 v34, 16, v34
	v_lshrrev_b32_e32 v6, 16, v6
	v_add3_u32 v7, v7, v39, s39
	v_lshrrev_b32_e32 v35, 16, v35
	v_and_or_b32 v8, v8, s38, v6
	v_and_or_b32 v6, v41, s38, v34
	v_mul_f32_e32 v34, v68, v59
	v_and_b32_e32 v37, 0xffff0000, v11
	v_and_b32_e32 v36, 0xffff0000, v10
	v_and_b32_e32 v39, 0xffff0000, v13
	v_and_b32_e32 v38, 0xffff0000, v12
	v_lshrrev_b32_e32 v7, 16, v7
	v_pk_mul_f32 v[36:37], v[34:35], v[36:37] op_sel_hi:[0,1]
	v_lshlrev_b32_e32 v11, 16, v11
	v_lshlrev_b32_e32 v10, 16, v10
	v_pk_mul_f32 v[38:39], v[34:35], v[38:39] op_sel_hi:[0,1]
	v_lshlrev_b32_e32 v13, 16, v13
	v_lshlrev_b32_e32 v12, 16, v12
	v_and_or_b32 v9, v9, s38, v7
	v_and_or_b32 v7, v40, s38, v35
	v_pk_mul_f32 v[10:11], v[34:35], v[10:11] op_sel_hi:[0,1]
	v_pk_mul_f32 v[12:13], v[34:35], v[12:13] op_sel_hi:[0,1]
	v_bfe_u32 v35, v39, 16, 1
	v_bfe_u32 v40, v38, 16, 1
	v_bfe_u32 v41, v37, 16, 1
	v_add3_u32 v37, v37, v41, s39
	v_add3_u32 v38, v38, v40, s39
	v_add3_u32 v35, v39, v35, s39
	v_bfe_u32 v39, v10, 16, 1
	v_bfe_u32 v40, v11, 16, 1
	v_bfe_u32 v41, v12, 16, 1
	v_bfe_u32 v60, v36, 16, 1
	v_add3_u32 v12, v12, v41, s39
	v_add3_u32 v11, v11, v40, s39
	v_add3_u32 v10, v10, v39, s39
	v_add3_u32 v36, v36, v60, s39
	v_bfe_u32 v60, v13, 16, 1
	v_lshrrev_b32_e32 v10, 16, v10
	v_lshrrev_b32_e32 v11, 16, v11
	v_lshrrev_b32_e32 v12, 16, v12
	v_add3_u32 v13, v13, v60, s39
	v_and_or_b32 v12, v38, s38, v12
	v_and_or_b32 v11, v37, s38, v11
	v_and_or_b32 v10, v36, s38, v10
	v_and_b32_e32 v37, 0xffff0000, v15
	v_and_b32_e32 v36, 0xffff0000, v14
	v_and_b32_e32 v39, 0xffff0000, v17
	v_and_b32_e32 v38, 0xffff0000, v16
	v_lshrrev_b32_e32 v13, 16, v13
	v_pk_mul_f32 v[36:37], v[34:35], v[36:37] op_sel_hi:[0,1]
	v_lshlrev_b32_e32 v15, 16, v15
	v_lshlrev_b32_e32 v14, 16, v14
	v_pk_mul_f32 v[38:39], v[34:35], v[38:39] op_sel_hi:[0,1]
	v_lshlrev_b32_e32 v17, 16, v17
	v_lshlrev_b32_e32 v16, 16, v16
	v_and_or_b32 v13, v35, s38, v13
	v_pk_mul_f32 v[14:15], v[34:35], v[14:15] op_sel_hi:[0,1]
	v_pk_mul_f32 v[16:17], v[34:35], v[16:17] op_sel_hi:[0,1]
	v_bfe_u32 v34, v39, 16, 1
	v_bfe_u32 v35, v38, 16, 1
	v_bfe_u32 v41, v36, 16, 1
	v_add3_u32 v36, v36, v41, s39
	v_add3_u32 v35, v38, v35, s39
	v_add3_u32 v34, v39, v34, s39
	v_bfe_u32 v38, v14, 16, 1
	v_bfe_u32 v39, v15, 16, 1
	v_bfe_u32 v41, v17, 16, 1
	v_bfe_u32 v40, v37, 16, 1
	v_add3_u32 v17, v17, v41, s39
	v_add3_u32 v15, v15, v39, s39
	v_add3_u32 v14, v14, v38, s39
	v_add3_u32 v37, v37, v40, s39
	v_bfe_u32 v40, v16, 16, 1
	v_lshrrev_b32_e32 v14, 16, v14
	v_lshrrev_b32_e32 v15, 16, v15
	v_lshrrev_b32_e32 v17, 16, v17
	v_add3_u32 v16, v16, v40, s39
	v_and_or_b32 v17, v34, s38, v17
	v_and_or_b32 v15, v37, s38, v15
	v_and_or_b32 v14, v36, s38, v14
	v_mul_f32_e32 v34, v67, v59
	v_and_b32_e32 v37, 0xffff0000, v19
	v_and_b32_e32 v36, 0xffff0000, v18
	v_and_b32_e32 v39, 0xffff0000, v21
	v_and_b32_e32 v38, 0xffff0000, v20
	v_lshrrev_b32_e32 v16, 16, v16
	v_pk_mul_f32 v[36:37], v[34:35], v[36:37] op_sel_hi:[0,1]
	v_lshlrev_b32_e32 v19, 16, v19
	v_lshlrev_b32_e32 v18, 16, v18
	v_pk_mul_f32 v[38:39], v[34:35], v[38:39] op_sel_hi:[0,1]
	v_lshlrev_b32_e32 v21, 16, v21
	v_lshlrev_b32_e32 v20, 16, v20
	v_and_or_b32 v16, v35, s38, v16
	v_pk_mul_f32 v[18:19], v[34:35], v[18:19] op_sel_hi:[0,1]
	v_pk_mul_f32 v[20:21], v[34:35], v[20:21] op_sel_hi:[0,1]
	v_bfe_u32 v35, v39, 16, 1
	v_bfe_u32 v40, v38, 16, 1
	v_bfe_u32 v41, v37, 16, 1
	v_add3_u32 v37, v37, v41, s39
	v_add3_u32 v38, v38, v40, s39
	v_add3_u32 v35, v39, v35, s39
	v_bfe_u32 v39, v18, 16, 1
	v_bfe_u32 v40, v19, 16, 1
	v_bfe_u32 v41, v20, 16, 1
	v_bfe_u32 v60, v36, 16, 1
	v_add3_u32 v20, v20, v41, s39
	v_add3_u32 v19, v19, v40, s39
	v_add3_u32 v18, v18, v39, s39
	v_add3_u32 v36, v36, v60, s39
	v_bfe_u32 v60, v21, 16, 1
	v_lshrrev_b32_e32 v18, 16, v18
	v_lshrrev_b32_e32 v19, 16, v19
	v_lshrrev_b32_e32 v20, 16, v20
	v_add3_u32 v21, v21, v60, s39
	v_and_or_b32 v20, v38, s38, v20
	v_and_or_b32 v19, v37, s38, v19
	v_and_or_b32 v18, v36, s38, v18
	v_and_b32_e32 v37, 0xffff0000, v23
	v_and_b32_e32 v36, 0xffff0000, v22
	v_and_b32_e32 v39, 0xffff0000, v25
	v_and_b32_e32 v38, 0xffff0000, v24
	v_lshrrev_b32_e32 v21, 16, v21
	v_pk_mul_f32 v[36:37], v[34:35], v[36:37] op_sel_hi:[0,1]
	v_lshlrev_b32_e32 v23, 16, v23
	v_lshlrev_b32_e32 v22, 16, v22
	v_pk_mul_f32 v[38:39], v[34:35], v[38:39] op_sel_hi:[0,1]
	v_lshlrev_b32_e32 v25, 16, v25
	v_lshlrev_b32_e32 v24, 16, v24
	v_and_or_b32 v21, v35, s38, v21
	v_pk_mul_f32 v[22:23], v[34:35], v[22:23] op_sel_hi:[0,1]
	v_pk_mul_f32 v[24:25], v[34:35], v[24:25] op_sel_hi:[0,1]
	v_bfe_u32 v34, v39, 16, 1
	v_bfe_u32 v35, v38, 16, 1
	v_bfe_u32 v41, v36, 16, 1
	v_add3_u32 v36, v36, v41, s39
	v_add3_u32 v35, v38, v35, s39
	v_add3_u32 v34, v39, v34, s39
	v_bfe_u32 v38, v22, 16, 1
	v_bfe_u32 v39, v23, 16, 1
	v_bfe_u32 v41, v25, 16, 1
	v_bfe_u32 v40, v37, 16, 1
	v_add3_u32 v25, v25, v41, s39
	v_add3_u32 v23, v23, v39, s39
	v_add3_u32 v22, v22, v38, s39
	v_add3_u32 v37, v37, v40, s39
	v_lshrrev_b32_e32 v22, 16, v22
	v_lshrrev_b32_e32 v23, 16, v23
	v_lshrrev_b32_e32 v25, 16, v25
	v_bfe_u32 v40, v24, 16, 1
	v_and_or_b32 v25, v34, s38, v25
	v_and_or_b32 v23, v37, s38, v23
	v_and_or_b32 v22, v36, s38, v22
	v_mul_f32_e32 v34, v66, v59
	v_and_b32_e32 v37, 0xffff0000, v27
	v_and_b32_e32 v36, 0xffff0000, v26
	v_add3_u32 v24, v24, v40, s39
	v_pk_mul_f32 v[36:37], v[34:35], v[36:37] op_sel_hi:[0,1]
	v_and_b32_e32 v39, 0xffff0000, v29
	v_and_b32_e32 v38, 0xffff0000, v28
	v_lshlrev_b32_e32 v29, 16, v29
	v_lshlrev_b32_e32 v28, 16, v28
	v_lshrrev_b32_e32 v24, 16, v24
	v_lshlrev_b32_e32 v27, 16, v27
	v_lshlrev_b32_e32 v26, 16, v26
	v_pk_mul_f32 v[38:39], v[34:35], v[38:39] op_sel_hi:[0,1]
	v_pk_mul_f32 v[28:29], v[34:35], v[28:29] op_sel_hi:[0,1]
	v_bfe_u32 v41, v37, 16, 1
	v_and_or_b32 v24, v35, s38, v24
	v_pk_mul_f32 v[26:27], v[34:35], v[26:27] op_sel_hi:[0,1]
	v_bfe_u32 v35, v39, 16, 1
	v_bfe_u32 v40, v38, 16, 1
	v_add3_u32 v37, v37, v41, s39
	v_bfe_u32 v41, v28, 16, 1
	v_bfe_u32 v59, v36, 16, 1
	v_add3_u32 v38, v38, v40, s39
	v_add3_u32 v35, v39, v35, s39
	v_bfe_u32 v39, v26, 16, 1
	v_bfe_u32 v40, v27, 16, 1
	v_add3_u32 v28, v28, v41, s39
	v_add3_u32 v36, v36, v59, s39
	v_bfe_u32 v59, v29, 16, 1
	v_add3_u32 v27, v27, v40, s39
	v_add3_u32 v26, v26, v39, s39
	v_lshrrev_b32_e32 v28, 16, v28
	v_add3_u32 v29, v29, v59, s39
	v_lshrrev_b32_e32 v26, 16, v26
	v_lshrrev_b32_e32 v27, 16, v27
	v_and_or_b32 v28, v38, s38, v28
	v_and_b32_e32 v39, 0xffff0000, v33
	v_and_b32_e32 v38, 0xffff0000, v32
	v_lshrrev_b32_e32 v29, 16, v29
	v_and_or_b32 v27, v37, s38, v27
	v_and_or_b32 v26, v36, s38, v26
	v_and_b32_e32 v37, 0xffff0000, v31
	v_and_b32_e32 v36, 0xffff0000, v30
	v_lshlrev_b32_e32 v31, 16, v31
	v_lshlrev_b32_e32 v30, 16, v30
	v_pk_mul_f32 v[38:39], v[34:35], v[38:39] op_sel_hi:[0,1]
	v_lshlrev_b32_e32 v33, 16, v33
	v_lshlrev_b32_e32 v32, 16, v32
	v_and_or_b32 v29, v35, s38, v29
	v_pk_mul_f32 v[36:37], v[34:35], v[36:37] op_sel_hi:[0,1]
	v_pk_mul_f32 v[30:31], v[34:35], v[30:31] op_sel_hi:[0,1]
	v_pk_mul_f32 v[32:33], v[34:35], v[32:33] op_sel_hi:[0,1]
	v_bfe_u32 v34, v39, 16, 1
	v_bfe_u32 v35, v38, 16, 1
	v_add3_u32 v35, v38, v35, s39
	v_add3_u32 v34, v39, v34, s39
	v_bfe_u32 v38, v30, 16, 1
	v_bfe_u32 v39, v31, 16, 1
	v_add3_u32 v31, v31, v39, s39
	v_add3_u32 v30, v30, v38, s39
	v_and_b32_e32 v38, -16, v42
	v_lshlrev_b32_e32 v39, 4, v232
	v_bfe_u32 v41, v36, 16, 1
	s_add_i32 s12, s50, -1
	v_bitop3_b32 v61, v39, v38, s0 bitop3:0x6c
	v_add_u32_e32 v38, 64, v38
	v_add3_u32 v36, v36, v41, s39
	v_bfe_u32 v41, v33, 16, 1
	v_bitop3_b32 v38, v39, v38, s0 bitop3:0x6c
	s_lshl_b32 s0, s12, 5
	v_add3_u32 v33, v33, v41, s39
	v_lshlrev_b32_e32 v59, 7, v232
	v_ashrrev_i32_e32 v41, 2, v42
	s_add_i32 s0, s0, s30
	v_bfe_u32 v40, v37, 16, 1
	v_and_b32_e32 v60, -4, v41
	v_add3_u32 v41, v38, v59, s1
	v_add3_u32 v59, v61, v59, s1
	s_ashr_i32 s1, s0, 31
	v_add3_u32 v37, v37, v40, s39
	v_bfe_u32 v40, v32, 16, 1
	s_lshl_b64 s[0:1], s[0:1], 9
	v_add3_u32 v32, v32, v40, s39
	v_lshrrev_b32_e32 v30, 16, v30
	v_lshrrev_b32_e32 v31, 16, v31
	s_add_u32 s0, s4, s0
	v_lshrrev_b32_e32 v32, 16, v32
	v_lshrrev_b32_e32 v33, 16, v33
	v_and_or_b32 v31, v37, s38, v31
	v_and_or_b32 v30, v36, s38, v30
	v_lshlrev_b64 v[36:37], 3, v[42:43]
	s_addc_u32 s1, s5, s1
	v_and_or_b32 v33, v34, s38, v33
	v_and_or_b32 v32, v35, s38, v32
	v_lshl_add_u64 v[34:35], s[4:5], 0, v[36:37]
	v_lshl_add_u64 v[36:37], s[0:1], 0, v[36:37]
	s_lshl_b32 s0, s50, 7
	v_readlane_b32 s1, v254, 10
	s_add_i32 s0, s1, s0
	v_lshl_add_u32 v40, v0, 10, 0
	v_add_u32_e32 v60, s0, v60
	s_mov_b32 s0, 0
	s_waitcnt vmcnt(0)
	s_branch .LBB0_500
